# phase 3 combine: four items per thread unrolled, 24 loads up front with counted waits
# baseline (speedup 1.0000x reference)
; DI void combine_phase(const bf16* outg, const float* lse, unsigned char* ycat, int gtid, int gthreads) {
;     for (int idx = gtid; idx < SEQ * 64; idx += gthreads) {
;         const int t = idx >> 6, ch = idx & 63, hh = ch >> 4, dd = (ch & 15) * 8;
;         const float l0 = lse[((size_t)0 * SEQ + t) * 4 + hh], l1 = lse[((size_t)1 * SEQ + t) * 4 + hh], l2 = lse[((size_t)2 * SEQ + t) * 4 + hh];
;         const float m = fmaxf(l0, fmaxf(l1, l2));
;         float w0 = __expf(l0 - m), w1 = __expf(l1 - m), w2 = __expf(l2 - m); const float rs = 1.0f / (w0 + w1 + w2); w0 *= rs; w1 *= rs; w2 *= rs;
;         const v4u a = *(const v4u*)(outg + ((size_t)0 * SEQ + t) * 512 + hh * 128 + dd);
;         const v4u b = *(const v4u*)(outg + ((size_t)1 * SEQ + t) * 512 + hh * 128 + dd);
;         const v4u c = *(const v4u*)(outg + ((size_t)2 * SEQ + t) * 512 + hh * 128 + dd);
;         w0 *= YSCALE; w1 *= YSCALE; w2 *= YSCALE;
;         v2u o;
;         o.x = pk4_fp8(w0 * bflo(a.x) + w1 * bflo(b.x) + w2 * bflo(c.x), w0 * bfhi(a.x) + w1 * bfhi(b.x) + w2 * bfhi(c.x), w0 * bflo(a.y) + w1 * bflo(b.y) + w2 * bflo(c.y), w0 * bfhi(a.y) + w1 * bfhi(b.y) + w2 * bfhi(c.y));
;         o.y = pk4_fp8(w0 * bflo(a.z) + w1 * bflo(b.z) + w2 * bflo(c.z), w0 * bfhi(a.z) + w1 * bfhi(b.z) + w2 * bfhi(c.z), w0 * bflo(a.w) + w1 * bflo(b.w) + w2 * bflo(c.w), w0 * bfhi(a.w) + w1 * bfhi(b.w) + w2 * bfhi(c.w));
;         *(v2u*)(ycat + (size_t)t * YCW + hh * 128 + dd) = o;
.LBB0_550:
	v_mov_b32_e32 v53, 0
	v_mov_b32_e32 v103, 0
	v_mov_b32_e32 v153, 0
	v_ashrrev_i32_e32 v12, 6, v8
	v_ashrrev_i32_e32 v13, 31, v12
	v_bfe_u32 v11, v8, 4, 2
	v_lshl_add_u64 v[20:21], v[12:13], 0, s[14:15]
	v_lshlrev_b32_e32 v2, 2, v11
	v_lshl_add_u64 v[18:19], v[12:13], 4, s[8:9]
	v_lshl_add_u64 v[22:23], v[12:13], 0, s[22:23]
	v_lshl_add_u64 v[28:29], v[20:21], 4, s[8:9]
	v_lshl_add_u64 v[18:19], v[18:19], 0, v[2:3]
	v_lshl_add_u64 v[30:31], v[22:23], 4, s[8:9]
	v_lshl_add_u64 v[28:29], v[28:29], 0, v[2:3]
	v_mad_i64_i32 v[26:27], s[26:27], v12, s11, v[4:5]
	v_lshlrev_b64 v[12:13], 10, v[12:13]
	v_lshlrev_b64 v[20:21], 10, v[20:21]
	v_lshlrev_b64 v[22:23], 10, v[22:23]
	v_lshl_add_u64 v[30:31], v[30:31], 0, v[2:3]
	global_load_dword v2, v[18:19], off
	s_nop 0
	global_load_dword v28, v[28:29], off
	s_nop 0
	global_load_dword v29, v[30:31], off
	v_and_b32_e32 v6, 0x78, v9
	v_mov_b32_e32 v15, v3
	v_lshlrev_b32_e32 v14, 8, v11
	v_lshl_add_u64 v[12:13], s[20:21], 0, v[12:13]
	v_lshl_add_u64 v[20:21], s[20:21], 0, v[20:21]
	v_lshl_add_u64 v[22:23], s[20:21], 0, v[22:23]
	v_mov_b32_e32 v17, v3
	v_lshlrev_b32_e32 v16, 1, v6
	v_lshl_add_u64 v[12:13], v[12:13], 0, v[14:15]
	v_lshl_add_u64 v[18:19], v[20:21], 0, v[14:15]
	v_lshl_add_u64 v[20:21], v[22:23], 0, v[14:15]
	v_lshl_add_u64 v[12:13], v[12:13], 0, v[16:17]
	v_lshl_add_u64 v[18:19], v[18:19], 0, v[16:17]
	v_lshl_add_u64 v[20:21], v[20:21], 0, v[16:17]
	global_load_dwordx4 v[12:15], v[12:13], off
	s_nop 0
	global_load_dwordx4 v[16:19], v[18:19], off
	s_nop 0
	global_load_dwordx4 v[20:23], v[20:21], off
	v_add_u32_e32 v8, s0, v8
	v_cmp_lt_i32_e32 vcc, s25, v8
	s_or_b64 s[6:7], vcc, s[6:7]
	v_mov_b32_e32 v24, v3
	v_mov_b32_e32 v25, v3
	v_mov_b32_e32 v7, v3
	v_add_u32_e32 v9, s1, v9
	v_ashrrev_i32_e32 v62, 6, v8
	v_ashrrev_i32_e32 v63, 31, v62
	v_bfe_u32 v61, v8, 4, 2
	v_lshl_add_u64 v[70:71], v[62:63], 0, s[14:15]
	v_lshlrev_b32_e32 v52, 2, v61
	v_lshl_add_u64 v[68:69], v[62:63], 4, s[8:9]
	v_lshl_add_u64 v[72:73], v[62:63], 0, s[22:23]
	v_lshl_add_u64 v[78:79], v[70:71], 4, s[8:9]
	v_lshl_add_u64 v[68:69], v[68:69], 0, v[52:53]
	v_lshl_add_u64 v[80:81], v[72:73], 4, s[8:9]
	v_lshl_add_u64 v[78:79], v[78:79], 0, v[52:53]
	v_mad_i64_i32 v[76:77], s[26:27], v62, s11, v[4:5]
	v_lshlrev_b64 v[62:63], 10, v[62:63]
	v_lshlrev_b64 v[70:71], 10, v[70:71]
	v_lshlrev_b64 v[72:73], 10, v[72:73]
	v_lshl_add_u64 v[80:81], v[80:81], 0, v[52:53]
	global_load_dword v52, v[68:69], off
	s_nop 0
	global_load_dword v78, v[78:79], off
	s_nop 0
	global_load_dword v79, v[80:81], off
	v_and_b32_e32 v56, 0x78, v9
	v_mov_b32_e32 v65, v3
	v_lshlrev_b32_e32 v64, 8, v61
	v_lshl_add_u64 v[62:63], s[20:21], 0, v[62:63]
	v_lshl_add_u64 v[70:71], s[20:21], 0, v[70:71]
	v_lshl_add_u64 v[72:73], s[20:21], 0, v[72:73]
	v_mov_b32_e32 v67, v3
	v_lshlrev_b32_e32 v66, 1, v56
	v_lshl_add_u64 v[62:63], v[62:63], 0, v[64:65]
	v_lshl_add_u64 v[68:69], v[70:71], 0, v[64:65]
	v_lshl_add_u64 v[70:71], v[72:73], 0, v[64:65]
	v_lshl_add_u64 v[62:63], v[62:63], 0, v[66:67]
	v_lshl_add_u64 v[68:69], v[68:69], 0, v[66:67]
	v_lshl_add_u64 v[70:71], v[70:71], 0, v[66:67]
	global_load_dwordx4 v[62:65], v[62:63], off
	s_nop 0
	global_load_dwordx4 v[66:69], v[68:69], off
	s_nop 0
	global_load_dwordx4 v[70:73], v[70:71], off
	v_add_u32_e32 v8, s0, v8
	v_cmp_lt_i32_e32 vcc, s25, v8
	s_or_b64 s[6:7], vcc, s[6:7]
	v_mov_b32_e32 v74, v3
	v_mov_b32_e32 v75, v3
	v_mov_b32_e32 v57, v3
	v_add_u32_e32 v9, s1, v9
	v_ashrrev_i32_e32 v112, 6, v8
	v_ashrrev_i32_e32 v113, 31, v112
	v_bfe_u32 v111, v8, 4, 2
	v_lshl_add_u64 v[120:121], v[112:113], 0, s[14:15]
	v_lshlrev_b32_e32 v102, 2, v111
	v_lshl_add_u64 v[118:119], v[112:113], 4, s[8:9]
	v_lshl_add_u64 v[122:123], v[112:113], 0, s[22:23]
	v_lshl_add_u64 v[128:129], v[120:121], 4, s[8:9]
	v_lshl_add_u64 v[118:119], v[118:119], 0, v[102:103]
	v_lshl_add_u64 v[130:131], v[122:123], 4, s[8:9]
	v_lshl_add_u64 v[128:129], v[128:129], 0, v[102:103]
	v_mad_i64_i32 v[126:127], s[26:27], v112, s11, v[4:5]
	v_lshlrev_b64 v[112:113], 10, v[112:113]
	v_lshlrev_b64 v[120:121], 10, v[120:121]
	v_lshlrev_b64 v[122:123], 10, v[122:123]
	v_lshl_add_u64 v[130:131], v[130:131], 0, v[102:103]
	global_load_dword v102, v[118:119], off
	s_nop 0
	global_load_dword v128, v[128:129], off
	s_nop 0
	global_load_dword v129, v[130:131], off
	v_and_b32_e32 v106, 0x78, v9
	v_mov_b32_e32 v115, v3
	v_lshlrev_b32_e32 v114, 8, v111
	v_lshl_add_u64 v[112:113], s[20:21], 0, v[112:113]
	v_lshl_add_u64 v[120:121], s[20:21], 0, v[120:121]
	v_lshl_add_u64 v[122:123], s[20:21], 0, v[122:123]
	v_mov_b32_e32 v117, v3
	v_lshlrev_b32_e32 v116, 1, v106
	v_lshl_add_u64 v[112:113], v[112:113], 0, v[114:115]
	v_lshl_add_u64 v[118:119], v[120:121], 0, v[114:115]
	v_lshl_add_u64 v[120:121], v[122:123], 0, v[114:115]
	v_lshl_add_u64 v[112:113], v[112:113], 0, v[116:117]
	v_lshl_add_u64 v[118:119], v[118:119], 0, v[116:117]
	v_lshl_add_u64 v[120:121], v[120:121], 0, v[116:117]
	global_load_dwordx4 v[112:115], v[112:113], off
	s_nop 0
	global_load_dwordx4 v[116:119], v[118:119], off
	s_nop 0
	global_load_dwordx4 v[120:123], v[120:121], off
	v_add_u32_e32 v8, s0, v8
	v_cmp_lt_i32_e32 vcc, s25, v8
	s_or_b64 s[6:7], vcc, s[6:7]
	v_mov_b32_e32 v124, v3
	v_mov_b32_e32 v125, v3
	v_mov_b32_e32 v107, v3
	v_add_u32_e32 v9, s1, v9
	v_ashrrev_i32_e32 v162, 6, v8
	v_ashrrev_i32_e32 v163, 31, v162
	v_bfe_u32 v161, v8, 4, 2
	v_lshl_add_u64 v[170:171], v[162:163], 0, s[14:15]
	v_lshlrev_b32_e32 v152, 2, v161
	v_lshl_add_u64 v[168:169], v[162:163], 4, s[8:9]
	v_lshl_add_u64 v[172:173], v[162:163], 0, s[22:23]
	v_lshl_add_u64 v[178:179], v[170:171], 4, s[8:9]
; DI void combine_phase(const bf16* outg, const float* lse, unsigned char* ycat, int gtid, int gthreads) {
;     for (int idx = gtid; idx < SEQ * 64; idx += gthreads) {
;         const int t = idx >> 6, ch = idx & 63, hh = ch >> 4, dd = (ch & 15) * 8;
;         const float l0 = lse[((size_t)0 * SEQ + t) * 4 + hh], l1 = lse[((size_t)1 * SEQ + t) * 4 + hh], l2 = lse[((size_t)2 * SEQ + t) * 4 + hh];
;         const float m = fmaxf(l0, fmaxf(l1, l2));
;         float w0 = __expf(l0 - m), w1 = __expf(l1 - m), w2 = __expf(l2 - m); const float rs = 1.0f / (w0 + w1 + w2); w0 *= rs; w1 *= rs; w2 *= rs;
;         const v4u a = *(const v4u*)(outg + ((size_t)0 * SEQ + t) * 512 + hh * 128 + dd);
;         const v4u b = *(const v4u*)(outg + ((size_t)1 * SEQ + t) * 512 + hh * 128 + dd);
;         const v4u c = *(const v4u*)(outg + ((size_t)2 * SEQ + t) * 512 + hh * 128 + dd);
;         w0 *= YSCALE; w1 *= YSCALE; w2 *= YSCALE;
;         v2u o;
;         o.x = pk4_fp8(w0 * bflo(a.x) + w1 * bflo(b.x) + w2 * bflo(c.x), w0 * bfhi(a.x) + w1 * bfhi(b.x) + w2 * bfhi(c.x), w0 * bflo(a.y) + w1 * bflo(b.y) + w2 * bflo(c.y), w0 * bfhi(a.y) + w1 * bfhi(b.y) + w2 * bfhi(c.y));
;         o.y = pk4_fp8(w0 * bflo(a.z) + w1 * bflo(b.z) + w2 * bflo(c.z), w0 * bfhi(a.z) + w1 * bfhi(b.z) + w2 * bfhi(c.z), w0 * bflo(a.w) + w1 * bflo(b.w) + w2 * bflo(c.w), w0 * bfhi(a.w) + w1 * bfhi(b.w) + w2 * bfhi(c.w));
;         *(v2u*)(ycat + (size_t)t * YCW + hh * 128 + dd) = o;
	v_lshl_add_u64 v[168:169], v[168:169], 0, v[152:153]
	v_lshl_add_u64 v[180:181], v[172:173], 4, s[8:9]
	v_lshl_add_u64 v[178:179], v[178:179], 0, v[152:153]
	v_mad_i64_i32 v[176:177], s[26:27], v162, s11, v[4:5]
	v_lshlrev_b64 v[162:163], 10, v[162:163]
	v_lshlrev_b64 v[170:171], 10, v[170:171]
	v_lshlrev_b64 v[172:173], 10, v[172:173]
	v_lshl_add_u64 v[180:181], v[180:181], 0, v[152:153]
	global_load_dword v152, v[168:169], off
	s_nop 0
	global_load_dword v178, v[178:179], off
	s_nop 0
	global_load_dword v179, v[180:181], off
	v_and_b32_e32 v156, 0x78, v9
	v_mov_b32_e32 v165, v3
	v_lshlrev_b32_e32 v164, 8, v161
	v_lshl_add_u64 v[162:163], s[20:21], 0, v[162:163]
	v_lshl_add_u64 v[170:171], s[20:21], 0, v[170:171]
	v_lshl_add_u64 v[172:173], s[20:21], 0, v[172:173]
	v_mov_b32_e32 v167, v3
	v_lshlrev_b32_e32 v166, 1, v156
	v_lshl_add_u64 v[162:163], v[162:163], 0, v[164:165]
	v_lshl_add_u64 v[168:169], v[170:171], 0, v[164:165]
	v_lshl_add_u64 v[170:171], v[172:173], 0, v[164:165]
	v_lshl_add_u64 v[162:163], v[162:163], 0, v[166:167]
	v_lshl_add_u64 v[168:169], v[168:169], 0, v[166:167]
	v_lshl_add_u64 v[170:171], v[170:171], 0, v[166:167]
	global_load_dwordx4 v[162:165], v[162:163], off
	s_nop 0
	global_load_dwordx4 v[166:169], v[168:169], off
	s_nop 0
	global_load_dwordx4 v[170:173], v[170:171], off
	v_add_u32_e32 v8, s0, v8
	v_cmp_lt_i32_e32 vcc, s25, v8
	s_or_b64 s[6:7], vcc, s[6:7]
	v_mov_b32_e32 v174, v3
	v_mov_b32_e32 v175, v3
	v_mov_b32_e32 v157, v3
	v_add_u32_e32 v9, s1, v9
	s_waitcnt vmcnt(21)
	v_max3_f32 v30, v2, v28, v29
	v_sub_f32_e32 v2, v2, v30
	v_sub_f32_e32 v28, v28, v30
	v_sub_f32_e32 v30, v29, v30
	v_mul_f32_e32 v2, 0x3fb8aa3b, v2
	v_mul_f32_e32 v40, 0x3fb8aa3b, v28
	v_mul_f32_e32 v41, 0x3fb8aa3b, v30
	s_waitcnt vmcnt(19)
	v_lshlrev_b32_e32 v44, 16, v17
	v_and_b32_e32 v45, 0xffff0000, v17
	v_lshlrev_b32_e32 v46, 16, v18
	v_and_b32_e32 v47, 0xffff0000, v18
	v_exp_f32_e32 v17, v2
	v_exp_f32_e32 v18, v40
	v_lshlrev_b32_e32 v42, 16, v16
	v_and_b32_e32 v43, 0xffff0000, v16
	v_exp_f32_e32 v16, v41
	v_add_f32_e32 v2, v17, v18
	v_lshlrev_b32_e32 v48, 16, v19
	v_and_b32_e32 v49, 0xffff0000, v19
	v_add_f32_e32 v2, v16, v2
	v_div_scale_f32 v19, s[26:27], v2, v2, 1.0
	v_lshlrev_b32_e32 v29, 16, v12
	v_and_b32_e32 v31, 0xffff0000, v12
	s_waitcnt vmcnt(18)
	v_lshlrev_b32_e32 v32, 16, v21
	v_and_b32_e32 v12, 0xffff0000, v21
	v_rcp_f32_e32 v21, v19
	v_lshlrev_b32_e32 v34, 16, v22
	v_and_b32_e32 v36, 0xffff0000, v22
	v_lshlrev_b32_e32 v28, 16, v20
	v_fma_f32 v22, -v19, v21, 1.0
	v_and_b32_e32 v30, 0xffff0000, v20
	v_div_scale_f32 v20, vcc, 1.0, v2, 1.0
	v_fmac_f32_e32 v21, v22, v21
	v_mul_f32_e32 v22, v20, v21
	v_lshlrev_b32_e32 v35, 16, v14
	v_and_b32_e32 v37, 0xffff0000, v14
	v_lshlrev_b32_e32 v38, 16, v23
	v_and_b32_e32 v14, 0xffff0000, v23
	v_fma_f32 v23, -v19, v22, v20
	v_fmac_f32_e32 v22, v23, v21
	v_fma_f32 v19, -v19, v22, v20
	v_div_fmas_f32 v19, v19, v21, v22
	v_div_fixup_f32 v2, v19, v2, 1.0
	v_pk_mul_f32 v[16:17], v[16:17], v[2:3] op_sel_hi:[1,0]
	v_lshlrev_b32_e32 v33, 16, v13
	v_and_b32_e32 v13, 0xffff0000, v13
	v_mul_f32_e32 v18, v18, v2
	v_pk_mul_f32 v[16:17], v[16:17], s[24:25] op_sel_hi:[1,0]
	v_lshlrev_b32_e32 v39, 16, v15
	v_and_b32_e32 v15, 0xffff0000, v15
	v_mul_f32_e32 v2, 0x42800000, v18
	v_pk_mul_f32 v[18:19], v[16:17], v[28:29]
	v_pk_mul_f32 v[20:21], v[16:17], v[30:31]
	v_pk_mul_f32 v[22:23], v[16:17], v[32:33]
	v_pk_mul_f32 v[12:13], v[16:17], v[12:13]
	v_pk_mul_f32 v[28:29], v[16:17], v[34:35]
	v_pk_mul_f32 v[30:31], v[16:17], v[36:37]
	v_pk_mul_f32 v[32:33], v[16:17], v[38:39]
	v_pk_mul_f32 v[14:15], v[16:17], v[14:15]
	v_fma_f32 v16, v2, v42, v19
	v_fma_f32 v17, v2, v43, v21
	v_fma_f32 v19, v2, v44, v23
	v_fma_f32 v13, v2, v45, v13
	v_fma_f32 v21, v2, v46, v29
	v_fma_f32 v23, v2, v47, v31
	v_fma_f32 v29, v2, v48, v33
	v_fma_f32 v2, v2, v49, v15
	v_add_f32_e32 v15, v18, v16
	v_add_f32_e32 v16, v20, v17
	v_add_f32_e32 v17, v22, v19
	v_add_f32_e32 v12, v12, v13
	v_add_f32_e32 v13, v28, v21
	v_add_f32_e32 v18, v30, v23
	v_add_f32_e32 v2, v14, v2
	v_med3_f32 v14, v15, s10, v10
	v_med3_f32 v15, v16, s10, v10
	v_med3_f32 v16, v17, s10, v10
	v_med3_f32 v13, v13, s10, v10
	v_med3_f32 v17, v18, s10, v10
	v_cvt_pk_fp8_f32 v24, v14, v15
	v_cvt_pk_fp8_f32 v25, v13, v17
	v_add_f32_e32 v19, v32, v29
	v_med3_f32 v12, v12, s10, v10
	v_med3_f32 v13, v19, s10, v10
	v_med3_f32 v2, v2, s10, v10
	v_cvt_pk_fp8_f32 v24, v16, v12 op_sel:[0,0,1]
	v_cvt_pk_fp8_f32 v25, v13, v2 op_sel:[0,0,1]
	v_lshlrev_b32_e32 v2, 7, v11
	v_lshl_add_u64 v[12:13], v[26:27], 0, v[2:3]
	v_lshl_add_u64 v[6:7], v[12:13], 0, v[6:7]
	global_store_dwordx2 v[6:7], v[24:25], off
	s_waitcnt vmcnt(16)
	v_max3_f32 v80, v52, v78, v79
	v_sub_f32_e32 v52, v52, v80
	v_sub_f32_e32 v78, v78, v80
	v_sub_f32_e32 v80, v79, v80
	v_mul_f32_e32 v52, 0x3fb8aa3b, v52
	v_mul_f32_e32 v90, 0x3fb8aa3b, v78
	v_mul_f32_e32 v91, 0x3fb8aa3b, v80
	s_waitcnt vmcnt(14)
	v_lshlrev_b32_e32 v94, 16, v67
	v_and_b32_e32 v95, 0xffff0000, v67
	v_lshlrev_b32_e32 v96, 16, v68
	v_and_b32_e32 v97, 0xffff0000, v68
	v_exp_f32_e32 v67, v52
	v_exp_f32_e32 v68, v90
	v_lshlrev_b32_e32 v92, 16, v66
	v_and_b32_e32 v93, 0xffff0000, v66
	v_exp_f32_e32 v66, v91
	v_add_f32_e32 v52, v67, v68
	v_lshlrev_b32_e32 v98, 16, v69
	v_and_b32_e32 v99, 0xffff0000, v69
	v_add_f32_e32 v52, v66, v52
	v_div_scale_f32 v69, s[26:27], v52, v52, 1.0
	v_lshlrev_b32_e32 v79, 16, v62
	v_and_b32_e32 v81, 0xffff0000, v62
	s_waitcnt vmcnt(13)
; DI void combine_phase(const bf16* outg, const float* lse, unsigned char* ycat, int gtid, int gthreads) {
;     for (int idx = gtid; idx < SEQ * 64; idx += gthreads) {
;         const int t = idx >> 6, ch = idx & 63, hh = ch >> 4, dd = (ch & 15) * 8;
;         const float l0 = lse[((size_t)0 * SEQ + t) * 4 + hh], l1 = lse[((size_t)1 * SEQ + t) * 4 + hh], l2 = lse[((size_t)2 * SEQ + t) * 4 + hh];
;         const float m = fmaxf(l0, fmaxf(l1, l2));
;         float w0 = __expf(l0 - m), w1 = __expf(l1 - m), w2 = __expf(l2 - m); const float rs = 1.0f / (w0 + w1 + w2); w0 *= rs; w1 *= rs; w2 *= rs;
;         const v4u a = *(const v4u*)(outg + ((size_t)0 * SEQ + t) * 512 + hh * 128 + dd);
;         const v4u b = *(const v4u*)(outg + ((size_t)1 * SEQ + t) * 512 + hh * 128 + dd);
;         const v4u c = *(const v4u*)(outg + ((size_t)2 * SEQ + t) * 512 + hh * 128 + dd);
;         w0 *= YSCALE; w1 *= YSCALE; w2 *= YSCALE;
;         v2u o;
;         o.x = pk4_fp8(w0 * bflo(a.x) + w1 * bflo(b.x) + w2 * bflo(c.x), w0 * bfhi(a.x) + w1 * bfhi(b.x) + w2 * bfhi(c.x), w0 * bflo(a.y) + w1 * bflo(b.y) + w2 * bflo(c.y), w0 * bfhi(a.y) + w1 * bfhi(b.y) + w2 * bfhi(c.y));
;         o.y = pk4_fp8(w0 * bflo(a.z) + w1 * bflo(b.z) + w2 * bflo(c.z), w0 * bfhi(a.z) + w1 * bfhi(b.z) + w2 * bfhi(c.z), w0 * bflo(a.w) + w1 * bflo(b.w) + w2 * bflo(c.w), w0 * bfhi(a.w) + w1 * bfhi(b.w) + w2 * bfhi(c.w));
;         *(v2u*)(ycat + (size_t)t * YCW + hh * 128 + dd) = o;
	v_lshlrev_b32_e32 v82, 16, v71
	v_and_b32_e32 v62, 0xffff0000, v71
	v_rcp_f32_e32 v71, v69
	v_lshlrev_b32_e32 v84, 16, v72
	v_and_b32_e32 v86, 0xffff0000, v72
	v_lshlrev_b32_e32 v78, 16, v70
	v_fma_f32 v72, -v69, v71, 1.0
	v_and_b32_e32 v80, 0xffff0000, v70
	v_div_scale_f32 v70, vcc, 1.0, v52, 1.0
	v_fmac_f32_e32 v71, v72, v71
	v_mul_f32_e32 v72, v70, v71
	v_lshlrev_b32_e32 v85, 16, v64
	v_and_b32_e32 v87, 0xffff0000, v64
	v_lshlrev_b32_e32 v88, 16, v73
	v_and_b32_e32 v64, 0xffff0000, v73
	v_fma_f32 v73, -v69, v72, v70
	v_fmac_f32_e32 v72, v73, v71
	v_fma_f32 v69, -v69, v72, v70
	v_div_fmas_f32 v69, v69, v71, v72
	v_div_fixup_f32 v52, v69, v52, 1.0
	v_pk_mul_f32 v[66:67], v[66:67], v[52:53] op_sel_hi:[1,0]
	v_lshlrev_b32_e32 v83, 16, v63
	v_and_b32_e32 v63, 0xffff0000, v63
	v_mul_f32_e32 v68, v68, v52
	v_pk_mul_f32 v[66:67], v[66:67], s[24:25] op_sel_hi:[1,0]
	v_lshlrev_b32_e32 v89, 16, v65
	v_and_b32_e32 v65, 0xffff0000, v65
	v_mul_f32_e32 v52, 0x42800000, v68
	v_pk_mul_f32 v[68:69], v[66:67], v[78:79]
	v_pk_mul_f32 v[70:71], v[66:67], v[80:81]
	v_pk_mul_f32 v[72:73], v[66:67], v[82:83]
	v_pk_mul_f32 v[62:63], v[66:67], v[62:63]
	v_pk_mul_f32 v[78:79], v[66:67], v[84:85]
	v_pk_mul_f32 v[80:81], v[66:67], v[86:87]
	v_pk_mul_f32 v[82:83], v[66:67], v[88:89]
	v_pk_mul_f32 v[64:65], v[66:67], v[64:65]
	v_fma_f32 v66, v52, v92, v69
	v_fma_f32 v67, v52, v93, v71
	v_fma_f32 v69, v52, v94, v73
	v_fma_f32 v63, v52, v95, v63
	v_fma_f32 v71, v52, v96, v79
	v_fma_f32 v73, v52, v97, v81
	v_fma_f32 v79, v52, v98, v83
	v_fma_f32 v52, v52, v99, v65
	v_add_f32_e32 v65, v68, v66
	v_add_f32_e32 v66, v70, v67
	v_add_f32_e32 v67, v72, v69
	v_add_f32_e32 v62, v62, v63
	v_add_f32_e32 v63, v78, v71
	v_add_f32_e32 v68, v80, v73
	v_add_f32_e32 v52, v64, v52
	v_med3_f32 v64, v65, s10, v10
	v_med3_f32 v65, v66, s10, v10
	v_med3_f32 v66, v67, s10, v10
	v_med3_f32 v63, v63, s10, v10
	v_med3_f32 v67, v68, s10, v10
	v_cvt_pk_fp8_f32 v74, v64, v65
	v_cvt_pk_fp8_f32 v75, v63, v67
	v_add_f32_e32 v69, v82, v79
	v_med3_f32 v62, v62, s10, v10
	v_med3_f32 v63, v69, s10, v10
	v_med3_f32 v52, v52, s10, v10
	v_cvt_pk_fp8_f32 v74, v66, v62 op_sel:[0,0,1]
	v_cvt_pk_fp8_f32 v75, v63, v52 op_sel:[0,0,1]
	v_lshlrev_b32_e32 v52, 7, v61
	v_lshl_add_u64 v[62:63], v[76:77], 0, v[52:53]
	v_lshl_add_u64 v[56:57], v[62:63], 0, v[56:57]
	global_store_dwordx2 v[56:57], v[74:75], off
	s_waitcnt vmcnt(11)
	v_max3_f32 v130, v102, v128, v129
	v_sub_f32_e32 v102, v102, v130
	v_sub_f32_e32 v128, v128, v130
	v_sub_f32_e32 v130, v129, v130
	v_mul_f32_e32 v102, 0x3fb8aa3b, v102
	v_mul_f32_e32 v140, 0x3fb8aa3b, v128
	v_mul_f32_e32 v141, 0x3fb8aa3b, v130
	s_waitcnt vmcnt(9)
	v_lshlrev_b32_e32 v144, 16, v117
	v_and_b32_e32 v145, 0xffff0000, v117
	v_lshlrev_b32_e32 v146, 16, v118
	v_and_b32_e32 v147, 0xffff0000, v118
	v_exp_f32_e32 v117, v102
	v_exp_f32_e32 v118, v140
	v_lshlrev_b32_e32 v142, 16, v116
	v_and_b32_e32 v143, 0xffff0000, v116
	v_exp_f32_e32 v116, v141
	v_add_f32_e32 v102, v117, v118
	v_lshlrev_b32_e32 v148, 16, v119
	v_and_b32_e32 v149, 0xffff0000, v119
	v_add_f32_e32 v102, v116, v102
	v_div_scale_f32 v119, s[26:27], v102, v102, 1.0
	v_lshlrev_b32_e32 v129, 16, v112
	v_and_b32_e32 v131, 0xffff0000, v112
	s_waitcnt vmcnt(8)
	v_lshlrev_b32_e32 v132, 16, v121
	v_and_b32_e32 v112, 0xffff0000, v121
	v_rcp_f32_e32 v121, v119
	v_lshlrev_b32_e32 v134, 16, v122
	v_and_b32_e32 v136, 0xffff0000, v122
	v_lshlrev_b32_e32 v128, 16, v120
	v_fma_f32 v122, -v119, v121, 1.0
	v_and_b32_e32 v130, 0xffff0000, v120
	v_div_scale_f32 v120, vcc, 1.0, v102, 1.0
	v_fmac_f32_e32 v121, v122, v121
	v_mul_f32_e32 v122, v120, v121
	v_lshlrev_b32_e32 v135, 16, v114
	v_and_b32_e32 v137, 0xffff0000, v114
	v_lshlrev_b32_e32 v138, 16, v123
	v_and_b32_e32 v114, 0xffff0000, v123
	v_fma_f32 v123, -v119, v122, v120
	v_fmac_f32_e32 v122, v123, v121
	v_fma_f32 v119, -v119, v122, v120
	v_div_fmas_f32 v119, v119, v121, v122
	v_div_fixup_f32 v102, v119, v102, 1.0
	v_pk_mul_f32 v[116:117], v[116:117], v[102:103] op_sel_hi:[1,0]
	v_lshlrev_b32_e32 v133, 16, v113
	v_and_b32_e32 v113, 0xffff0000, v113
	v_mul_f32_e32 v118, v118, v102
	v_pk_mul_f32 v[116:117], v[116:117], s[24:25] op_sel_hi:[1,0]
	v_lshlrev_b32_e32 v139, 16, v115
	v_and_b32_e32 v115, 0xffff0000, v115
	v_mul_f32_e32 v102, 0x42800000, v118
	v_pk_mul_f32 v[118:119], v[116:117], v[128:129]
	v_pk_mul_f32 v[120:121], v[116:117], v[130:131]
	v_pk_mul_f32 v[122:123], v[116:117], v[132:133]
	v_pk_mul_f32 v[112:113], v[116:117], v[112:113]
	v_pk_mul_f32 v[128:129], v[116:117], v[134:135]
	v_pk_mul_f32 v[130:131], v[116:117], v[136:137]
	v_pk_mul_f32 v[132:133], v[116:117], v[138:139]
	v_pk_mul_f32 v[114:115], v[116:117], v[114:115]
	v_fma_f32 v116, v102, v142, v119
	v_fma_f32 v117, v102, v143, v121
	v_fma_f32 v119, v102, v144, v123
	v_fma_f32 v113, v102, v145, v113
	v_fma_f32 v121, v102, v146, v129
	v_fma_f32 v123, v102, v147, v131
	v_fma_f32 v129, v102, v148, v133
	v_fma_f32 v102, v102, v149, v115
	v_add_f32_e32 v115, v118, v116
	v_add_f32_e32 v116, v120, v117
	v_add_f32_e32 v117, v122, v119
	v_add_f32_e32 v112, v112, v113
	v_add_f32_e32 v113, v128, v121
	v_add_f32_e32 v118, v130, v123
	v_add_f32_e32 v102, v114, v102
	v_med3_f32 v114, v115, s10, v10
	v_med3_f32 v115, v116, s10, v10
	v_med3_f32 v116, v117, s10, v10
	v_med3_f32 v113, v113, s10, v10
	v_med3_f32 v117, v118, s10, v10
	v_cvt_pk_fp8_f32 v124, v114, v115
	v_cvt_pk_fp8_f32 v125, v113, v117
	v_add_f32_e32 v119, v132, v129
	v_med3_f32 v112, v112, s10, v10
	v_med3_f32 v113, v119, s10, v10
	v_med3_f32 v102, v102, s10, v10
	v_cvt_pk_fp8_f32 v124, v116, v112 op_sel:[0,0,1]
	v_cvt_pk_fp8_f32 v125, v113, v102 op_sel:[0,0,1]
	v_lshlrev_b32_e32 v102, 7, v111
	v_lshl_add_u64 v[112:113], v[126:127], 0, v[102:103]
	v_lshl_add_u64 v[106:107], v[112:113], 0, v[106:107]
	global_store_dwordx2 v[106:107], v[124:125], off
	s_waitcnt vmcnt(6)
; DI void combine_phase(const bf16* outg, const float* lse, unsigned char* ycat, int gtid, int gthreads) {
;     for (int idx = gtid; idx < SEQ * 64; idx += gthreads) {
;         const int t = idx >> 6, ch = idx & 63, hh = ch >> 4, dd = (ch & 15) * 8;
;         const float l0 = lse[((size_t)0 * SEQ + t) * 4 + hh], l1 = lse[((size_t)1 * SEQ + t) * 4 + hh], l2 = lse[((size_t)2 * SEQ + t) * 4 + hh];
;         const float m = fmaxf(l0, fmaxf(l1, l2));
;         float w0 = __expf(l0 - m), w1 = __expf(l1 - m), w2 = __expf(l2 - m); const float rs = 1.0f / (w0 + w1 + w2); w0 *= rs; w1 *= rs; w2 *= rs;
;         const v4u a = *(const v4u*)(outg + ((size_t)0 * SEQ + t) * 512 + hh * 128 + dd);
;         const v4u b = *(const v4u*)(outg + ((size_t)1 * SEQ + t) * 512 + hh * 128 + dd);
;         const v4u c = *(const v4u*)(outg + ((size_t)2 * SEQ + t) * 512 + hh * 128 + dd);
;         w0 *= YSCALE; w1 *= YSCALE; w2 *= YSCALE;
;         v2u o;
;         o.x = pk4_fp8(w0 * bflo(a.x) + w1 * bflo(b.x) + w2 * bflo(c.x), w0 * bfhi(a.x) + w1 * bfhi(b.x) + w2 * bfhi(c.x), w0 * bflo(a.y) + w1 * bflo(b.y) + w2 * bflo(c.y), w0 * bfhi(a.y) + w1 * bfhi(b.y) + w2 * bfhi(c.y));
;         o.y = pk4_fp8(w0 * bflo(a.z) + w1 * bflo(b.z) + w2 * bflo(c.z), w0 * bfhi(a.z) + w1 * bfhi(b.z) + w2 * bfhi(c.z), w0 * bflo(a.w) + w1 * bflo(b.w) + w2 * bflo(c.w), w0 * bfhi(a.w) + w1 * bfhi(b.w) + w2 * bfhi(c.w));
;         *(v2u*)(ycat + (size_t)t * YCW + hh * 128 + dd) = o;
	v_max3_f32 v180, v152, v178, v179
	v_sub_f32_e32 v152, v152, v180
	v_sub_f32_e32 v178, v178, v180
	v_sub_f32_e32 v180, v179, v180
	v_mul_f32_e32 v152, 0x3fb8aa3b, v152
	v_mul_f32_e32 v190, 0x3fb8aa3b, v178
	v_mul_f32_e32 v191, 0x3fb8aa3b, v180
	s_waitcnt vmcnt(4)
	v_lshlrev_b32_e32 v194, 16, v167
	v_and_b32_e32 v195, 0xffff0000, v167
	v_lshlrev_b32_e32 v196, 16, v168
	v_and_b32_e32 v197, 0xffff0000, v168
	v_exp_f32_e32 v167, v152
	v_exp_f32_e32 v168, v190
	v_lshlrev_b32_e32 v192, 16, v166
	v_and_b32_e32 v193, 0xffff0000, v166
	v_exp_f32_e32 v166, v191
	v_add_f32_e32 v152, v167, v168
	v_lshlrev_b32_e32 v198, 16, v169
	v_and_b32_e32 v199, 0xffff0000, v169
	v_add_f32_e32 v152, v166, v152
	v_div_scale_f32 v169, s[26:27], v152, v152, 1.0
	v_lshlrev_b32_e32 v179, 16, v162
	v_and_b32_e32 v181, 0xffff0000, v162
	s_waitcnt vmcnt(3)
	v_lshlrev_b32_e32 v182, 16, v171
	v_and_b32_e32 v162, 0xffff0000, v171
	v_rcp_f32_e32 v171, v169
	v_lshlrev_b32_e32 v184, 16, v172
	v_and_b32_e32 v186, 0xffff0000, v172
	v_lshlrev_b32_e32 v178, 16, v170
	v_fma_f32 v172, -v169, v171, 1.0
	v_and_b32_e32 v180, 0xffff0000, v170
	v_div_scale_f32 v170, vcc, 1.0, v152, 1.0
	v_fmac_f32_e32 v171, v172, v171
	v_mul_f32_e32 v172, v170, v171
	v_lshlrev_b32_e32 v185, 16, v164
	v_and_b32_e32 v187, 0xffff0000, v164
	v_lshlrev_b32_e32 v188, 16, v173
	v_and_b32_e32 v164, 0xffff0000, v173
	v_fma_f32 v173, -v169, v172, v170
	v_fmac_f32_e32 v172, v173, v171
	v_fma_f32 v169, -v169, v172, v170
	v_div_fmas_f32 v169, v169, v171, v172
	v_div_fixup_f32 v152, v169, v152, 1.0
	v_pk_mul_f32 v[166:167], v[166:167], v[152:153] op_sel_hi:[1,0]
	v_lshlrev_b32_e32 v183, 16, v163
	v_and_b32_e32 v163, 0xffff0000, v163
	v_mul_f32_e32 v168, v168, v152
	v_pk_mul_f32 v[166:167], v[166:167], s[24:25] op_sel_hi:[1,0]
	v_lshlrev_b32_e32 v189, 16, v165
	v_and_b32_e32 v165, 0xffff0000, v165
	v_mul_f32_e32 v152, 0x42800000, v168
	v_pk_mul_f32 v[168:169], v[166:167], v[178:179]
	v_pk_mul_f32 v[170:171], v[166:167], v[180:181]
	v_pk_mul_f32 v[172:173], v[166:167], v[182:183]
	v_pk_mul_f32 v[162:163], v[166:167], v[162:163]
	v_pk_mul_f32 v[178:179], v[166:167], v[184:185]
	v_pk_mul_f32 v[180:181], v[166:167], v[186:187]
	v_pk_mul_f32 v[182:183], v[166:167], v[188:189]
	v_pk_mul_f32 v[164:165], v[166:167], v[164:165]
	v_fma_f32 v166, v152, v192, v169
	v_fma_f32 v167, v152, v193, v171
	v_fma_f32 v169, v152, v194, v173
	v_fma_f32 v163, v152, v195, v163
	v_fma_f32 v171, v152, v196, v179
	v_fma_f32 v173, v152, v197, v181
	v_fma_f32 v179, v152, v198, v183
	v_fma_f32 v152, v152, v199, v165
	v_add_f32_e32 v165, v168, v166
	v_add_f32_e32 v166, v170, v167
	v_add_f32_e32 v167, v172, v169
	v_add_f32_e32 v162, v162, v163
	v_add_f32_e32 v163, v178, v171
	v_add_f32_e32 v168, v180, v173
	v_add_f32_e32 v152, v164, v152
	v_med3_f32 v164, v165, s10, v10
	v_med3_f32 v165, v166, s10, v10
	v_med3_f32 v166, v167, s10, v10
	v_med3_f32 v163, v163, s10, v10
	v_med3_f32 v167, v168, s10, v10
	v_cvt_pk_fp8_f32 v174, v164, v165
	v_cvt_pk_fp8_f32 v175, v163, v167
	v_add_f32_e32 v169, v182, v179
	v_med3_f32 v162, v162, s10, v10
	v_med3_f32 v163, v169, s10, v10
	v_med3_f32 v152, v152, s10, v10
	v_cvt_pk_fp8_f32 v174, v166, v162 op_sel:[0,0,1]
	v_cvt_pk_fp8_f32 v175, v163, v152 op_sel:[0,0,1]
	v_lshlrev_b32_e32 v152, 7, v161
	v_lshl_add_u64 v[162:163], v[176:177], 0, v[152:153]
	v_lshl_add_u64 v[156:157], v[162:163], 0, v[156:157]
	global_store_dwordx2 v[156:157], v[174:175], off
